# speedup vs baseline: 1.0216x; 1.0141x over previous
.LBB1_98:
	s_andn2_b64 vcc, exec, s[36:37]
	s_cbranch_vccnz .LBB1_102
	v_accvgpr_read_b32 v14, a138
	v_accvgpr_read_b32 v15, a139
	v_fma_f32 v0, v14, v10, 0
	v_accvgpr_read_b32 v16, a140
	v_fmac_f32_e32 v0, v15, v11
	v_accvgpr_read_b32 v17, a141
	v_fmac_f32_e32 v0, v16, v12
	v_fmac_f32_e32 v0, v17, v13
	v_fma_f32 v10, v14, v6, 0
	v_fmac_f32_e32 v10, v15, v7
	v_fmac_f32_e32 v10, v16, v8
	v_fmac_f32_e32 v10, v17, v9
	v_mov_b32_e32 v3, v0
	v_mov_b32_e32 v1, v10
	s_nop 1
	v_permlane16_swap_b32_e32 v0, v3
	v_permlane16_swap_b32_e32 v10, v1
	v_add_f32_e32 v6, v0, v3
	v_add_f32_e32 v8, v10, v1
	v_mov_b32_e32 v7, v6
	v_mov_b32_e32 v9, v8
	s_nop 1
	v_permlane32_swap_b32_e32 v6, v7
	v_permlane32_swap_b32_e32 v8, v9
	s_and_saveexec_b64 s[36:37], s[10:11]
	s_cbranch_execz .LBB1_101
	v_accvgpr_read_b32 v2, a144
	v_accvgpr_read_b32 v3, a145
	v_add_u32_e32 v2, v2, v3
	s_waitcnt lgkmcnt(0)
	v_add_f32_e32 v0, v8, v9
	v_add_f32_e32 v1, v6, v7
	v_add_u32_e32 v2, 0x8400, v2
	ds_write2_b32 v2, v1, v0 offset0:64 offset1:80

.LBB1_162:
	s_add_i32 s40, s40, 4
	v_cvt_f16_f32_e32 v0, v6
	v_cvt_f16_f32_e32 v1, v7
	v_cvt_f16_f32_e32 v2, v8
	v_cvt_f16_f32_e32 v3, v9
	ds_write_b32 v184, v6 offset:25600
	ds_write_b16 v243, v0 offset:128
	ds_write_b32 v250, v7 offset:25600
	v_add_u32_e32 v0, 0x320, v243
	ds_write_b16 v0, v1 offset:128
	ds_write_b32 v185, v8 offset:25600
	v_add_u32_e32 v0, 0x640, v243
	ds_write_b16 v0, v2 offset:128
	ds_write_b32 v251, v9 offset:25600
	v_add_u32_e32 v0, 0x960, v243
	ds_write_b16 v0, v3 offset:128
	s_andn2_b64 vcc, exec, s[18:19]
	s_waitcnt lgkmcnt(0)
	s_barrier
	s_cbranch_vccnz .LBB1_74
	v_mul_f32_e32 v10, v112, v6
	v_mul_f32_e32 v11, v112, v7
	v_mul_f32_e32 v12, v112, v8
	v_mul_f32_e32 v13, v112, v9
	v_mov_b32_dpp v0, v10 quad_perm:[1,0,3,2] row_mask:0xf bank_mask:0xf
	v_mov_b32_dpp v1, v11 quad_perm:[1,0,3,2] row_mask:0xf bank_mask:0xf
	v_mov_b32_dpp v2, v12 quad_perm:[1,0,3,2] row_mask:0xf bank_mask:0xf
	v_mov_b32_dpp v3, v13 quad_perm:[1,0,3,2] row_mask:0xf bank_mask:0xf
	v_fmac_f32_e32 v0, v112, v6
	v_fmac_f32_e32 v1, v112, v7
	v_fmac_f32_e32 v2, v112, v8
	v_fmac_f32_e32 v3, v112, v9
	v_add_f32_dpp v0, v0, v0 quad_perm:[2,3,0,1] row_mask:0xf bank_mask:0xf
	v_add_f32_dpp v1, v1, v1 quad_perm:[2,3,0,1] row_mask:0xf bank_mask:0xf
	v_add_f32_dpp v2, v2, v2 quad_perm:[2,3,0,1] row_mask:0xf bank_mask:0xf
	v_add_f32_dpp v3, v3, v3 quad_perm:[2,3,0,1] row_mask:0xf bank_mask:0xf
	v_add_f32_dpp v0, v0, v0 row_shl:4 row_mask:0xf bank_mask:0xf
	v_add_f32_dpp v1, v1, v1 row_shl:4 row_mask:0xf bank_mask:0xf
	v_add_f32_dpp v2, v2, v2 row_shl:4 row_mask:0xf bank_mask:0xf
	v_add_f32_dpp v3, v3, v3 row_shl:4 row_mask:0xf bank_mask:0xf
	v_add_f32_dpp v0, v0, v0 row_shl:8 row_mask:0xf bank_mask:0xf
	v_add_f32_dpp v1, v1, v1 row_shl:8 row_mask:0xf bank_mask:0xf
	v_add_f32_dpp v2, v2, v2 row_shl:8 row_mask:0xf bank_mask:0xf
	v_add_f32_dpp v3, v3, v3 row_shl:8 row_mask:0xf bank_mask:0xf
	s_and_saveexec_b64 s[16:17], s[14:15]
	s_cbranch_execz .LBB1_169
	v_accvgpr_read_b32 v6, a240
	ds_write_b128 v6, v[0:3] offset:34560
